# adds: LN1 gain/bias staged in LDS, top-8 rewritten compactly with next group's second-half fragments requested behind B2, row-part waits recounted so the HBM row prefetch is waited where consumed
# speedup vs baseline: 1.0205x; 1.0040x over previous
; __device__ __forceinline__ void lds_barrier() { asm volatile("s_waitcnt lgkmcnt(0)" ::: "memory"); __builtin_amdgcn_s_barrier(); asm volatile("" ::: "memory"); }
; #define LN1_PREFETCH(g_) do { _Pragma("unroll") for (int rr = 0; rr < 2; ++rr) { const int R_ = (g_) * 16 + 2 * wave + rr; \
;         _Pragma("unroll") for (int j = 0; j < 4; ++j) nvb[rr][j] = __builtin_nontemporal_load((const v2u*)(VB16 + (size_t)R_ * D + 4 * lane + 256 * j)); } } while (0)
; __device__ __forceinline__ void phase_ln1(Frame& F0, const Args& A, int l, bool v_from_h) {
;     ...
;     if (F.vcu < ngroups) { LN1_PREFETCH(F.vcu); LN1_ROWPART(F.vcu, F.vcu + F.G); }
;     bf16x8 wh[4][4], wl[4][4];
;     const unsigned wloff = (unsigned)(fr * D + fq * 8) * 2u;
;     const char* rhb[4]; const char* rlb[4];
; #pragma unroll
;     for (int eg = 0; eg < 4; ++eg) { rhb[eg] = (const char*)(RH + wave * 128) + eg * 16 * D * 2; rlb[eg] = (const char*)(RL + wave * 128) + eg * 16 * D * 2; }
;     ...
;     LN1_GLDK(0); LN1_GLDK(1);
;     int pend_r[2] = {-1, -1}; float pend_w[2] = {0.f, 0.f};
;     ...
;     const float brl = brt[lane];
;     lds_barrier();
;     ...
;             for (int rr = 0; rr < 2; ++rr) { const bool sel = rank[rr] < 8; const float ssum = wave_sum(sel ? score[rr] : 0.f);
;                 pend_r[rr] = sel ? rank[rr] : -1; pend_w[rr] = score[rr] / ssum * ROUTED_SCALE; if (sel) atomicAdd((int*)&lhist[lane], 1); }
.LBB0_1283:
	s_lshl_b64 s[0:1], s[50:51], 2
	s_add_u32 s2, s24, s0
	s_addc_u32 s3, s25, s1
	v_readlane_b32 s0, v254, 44
	v_readlane_b32 s1, v254, 45
	s_lshl_b64 s[0:1], s[0:1], 17
	s_add_u32 s17, s22, s0
	s_addc_u32 s18, s23, s1
	s_add_u32 s6, s22, 0x600000
	s_addc_u32 s7, s23, 0
	s_add_u32 s8, s22, 0x800000
	s_addc_u32 s9, s23, 0
	s_lshl_b32 s0, s4, 7
	s_ashr_i32 s1, s0, 31
	s_lshl_b64 s[12:13], s[0:1], 1
	s_add_u32 s1, s17, s12
	s_addc_u32 s12, s18, s13
	s_add_u32 s20, s1, 0x400000
	s_addc_u32 s21, s12, 0
	s_add_u32 s24, s1, 0x480000
	s_addc_u32 s25, s12, 0
	s_add_u32 s26, s1, 0x408000
	s_addc_u32 s27, s12, 0
	s_add_u32 s42, s1, 0x488000
	v_and_b32_e32 v65, 15, v128
	v_and_b32_e32 v64, -16, v128
	s_addc_u32 s43, s12, 0
	s_nop 4
	s_add_u32 s50, s1, 0x410000
	v_lshl_add_u32 v219, v65, 11, v64
	global_load_dwordx4 v[0:3], v219, s[20:21] offset:0
	s_addc_u32 s51, s12, 0
	s_waitcnt vmcnt(0)
	global_load_dwordx4 v[4:7], v219, s[24:25] offset:0
	s_add_u32 s62, s1, 0x490000
	global_load_dwordx4 v[8:11], v219, s[26:27] offset:0
	s_addc_u32 s63, s12, 0
	global_load_dwordx4 v[12:15], v219, s[42:43] offset:0
	s_add_u32 s68, s1, 0x418000
	global_load_dwordx4 v[16:19], v219, s[50:51] offset:0
	s_addc_u32 s69, s12, 0
	global_load_dwordx4 v[20:23], v219, s[62:63] offset:0
	s_add_u32 s74, s1, 0x498000
	global_load_dwordx4 v[24:27], v219, s[68:69] offset:0
	s_addc_u32 s75, s12, 0
	global_load_dwordx4 v[28:31], v219, s[74:75] offset:0
	s_nop 4
	global_load_dwordx4 v[32:35], v219, s[20:21] offset:64
	global_load_dwordx4 v[36:39], v219, s[24:25] offset:64
	global_load_dwordx4 v[40:43], v219, s[26:27] offset:64
	global_load_dwordx4 v[44:47], v219, s[42:43] offset:64
	global_load_dwordx4 v[48:51], v219, s[50:51] offset:64
	global_load_dwordx4 v[52:55], v219, s[62:63] offset:64
	global_load_dwordx4 v[56:59], v219, s[68:69] offset:64
	v_ashrrev_i32_e32 v129, 31, v128
	global_load_dwordx4 v[60:63], v219, s[74:75] offset:64
	v_lshl_add_u64 v[66:67], v[128:129], 2, s[2:3]
	global_load_dword v148, v[66:67], off
	s_waitcnt lgkmcnt(0)
	s_barrier
	s_andn2_b64 vcc, exec, s[46:47]
	s_cbranch_vccnz .LBB0_1302
	v_lshrrev_b32_e32 v66, 1, v128
	v_and_b32_e32 v66, 0x7ffffff8, v66
	v_mul_u32_u24_e32 v67, 0x408, v65
	s_lshl_b32 s1, s4, 12
	v_readlane_b32 s2, v254, 33
	v_lshlrev_b32_e32 v67, 1, v67
	v_add_lshl_u32 v66, v66, s0, 1
	s_add_i32 s1, s2, s1
	v_add3_u32 v220, 0, v67, v66
	s_add_u32 s12, s22, 0x100000
	v_lshlrev_b64 v[66:67], 2, v[130:131]
	v_lshl_add_u32 v65, v65, 8, s1
	s_addc_u32 s13, s23, 0
	s_cmp_lt_u32 s4, 4
	s_cselect_b32 s40, s66, s94
	s_cselect_b32 s41, s67, s95
	s_and_b32 s1, s4, 3
	s_lshl_b32 s1, s1, 10
	s_add_u32 s40, s40, s1
	s_addc_u32 s41, s41, 0
	v_lshlrev_b32_e32 v74, 4, v128
	global_load_dwordx4 v[70:73], v74, s[40:41]
	s_lshl_b32 s1, s4, 10
	s_add_i32 s1, s1, 0x1a400
	v_add_u32_e32 v75, s1, v74
	v_add_u32_e32 v150, 0x1a400, v74
	s_lshl_b32 s1, s4, 1
	v_lshlrev_b64 v[66:67], 1, v[130:131]
	s_add_i32 s3, 0, 0x19200
	v_lshl_add_u64 v[154:155], s[14:15], 0, v[66:67]
	v_lshl_add_u64 v[66:67], s[22:23], 0, v[66:67]
	s_mov_b64 s[14:15], 0x2fc00000
	v_add_u32_e32 v223, s3, v130
	s_or_b32 s3, s1, 1
	v_lshl_add_u64 v[156:157], v[66:67], 0, s[14:15]
	v_lshl_add_u32 v66, v128, 3, 0
	s_mulk_i32 s3, 0x810
	v_readlane_b32 s14, v254, 34
	v_add_u32_e32 v224, s16, v66
	v_add_u32_e32 v225, s3, v66
	v_add_lshl_u32 v66, s0, v128, 2
	v_readlane_b32 s0, v254, 35
	v_add_u32_e32 v226, s14, v66
	v_lshlrev_b32_e32 v67, 3, v100
	v_add_u32_e32 v227, s0, v66
	v_add_u32_e32 v66, 0x100, v66
	v_add_u32_e32 v229, s0, v66
	v_readlane_b32 s0, v254, 14
	v_add_u32_e32 v221, s2, v67
	s_lshl_b32 s2, s4, 9
	s_add_i32 s16, s0, s1
	v_readlane_b32 s0, v254, 11
	v_sub_u32_e32 v160, 63, v128
	s_add_i32 s17, s0, s1
	v_readlane_b32 s0, v253, 29
	v_mov_b32_e32 v162, -1
	s_add_i32 s44, s2, 0
	v_lshl_add_u64 v[158:159], s[76:77], 0, v[130:131]
	v_add_u32_e32 v222, s14, v67
	v_add_u32_e32 v228, s14, v66
	s_waitcnt vmcnt(0)
	ds_write_b128 v75, v[70:73]
	v_mov_b32_e32 v149, v148
	v_mov_b32_e32 v129, v160
	s_add_i32 s18, s0, s1
	v_mov_b32_e32 v231, 0
	s_mov_b32 s19, 0
	v_add_u32_e32 v230, v65, v64
	s_add_i32 s44, s44, 0x19300
	s_mov_b32 s45, 0
	v_mov_b32_e32 v180, v162
	v_mov_b32_e32 v163, 0
	s_branch .Lln1_first
.LBB0_1285:
	s_or_b64 exec, exec, s[0:1]
	v_div_scale_f32 v166, s[0:1], s2, s2, v165
	v_rcp_f32_e32 v167, v166
	s_add_i32 s19, s19, s70
	v_fma_f32 v168, -v166, v167, 1.0
	v_fmac_f32_e32 v167, v168, v167
	v_div_scale_f32 v168, vcc, v165, s2, v165
	v_mul_f32_e32 v169, v168, v167
	v_fma_f32 v170, -v166, v169, v168
	v_fmac_f32_e32 v169, v170, v167
	v_fma_f32 v166, -v166, v169, v168
	v_div_fmas_f32 v166, v166, v167, v169
	v_div_fixup_f32 v166, v166, s2, v165
	v_mul_f32_e32 v163, 0x40200000, v166
	v_div_scale_f32 v166, s[0:1], s3, s3, v164
	v_rcp_f32_e32 v167, v166
	v_readlane_b32 s0, v254, 15
	s_add_i32 s45, s45, s0
	v_readlane_b32 s0, v254, 12
	v_fma_f32 v168, -v166, v167, 1.0
	v_fmac_f32_e32 v167, v168, v167
	v_div_scale_f32 v168, vcc, v164, s3, v164
	v_mul_f32_e32 v169, v168, v167
	v_fma_f32 v170, -v166, v169, v168
	v_fmac_f32_e32 v169, v170, v167
	v_fma_f32 v166, -v166, v169, v168
	v_div_fmas_f32 v166, v166, v167, v169
	v_div_fixup_f32 v166, v166, s3, v164
	s_add_i32 s0, s0, s19
	v_mul_f32_e32 v231, 0x40200000, v166
	s_cmp_ge_i32 s0, s5
	s_cbranch_scc1 .LBB0_1303
	s_branch .LBB0_1286

; #define LAS __attribute__((address_space(3)))
; __device__ __forceinline__ void lds_barrier() { asm volatile("s_waitcnt lgkmcnt(0)" ::: "memory"); __builtin_amdgcn_s_barrier(); asm volatile("" ::: "memory"); }
; __device__ __forceinline__ void phase_ln1(Frame& F0, const Args& A, int l, bool v_from_h) {
;     ...
;         {   LN1_GLDK(2); LN1_GLDK(3);
;             f32x4 acc[4];
; #pragma unroll
;             for (int eg = 0; eg < 4; ++eg) acc[eg] = (f32x4){0.f, 0.f, 0.f, 0.f};
;     ...
;             LN1_KSTEP(24, 0); LN1_KSTEP(16, 1); LN1_KSTEP(8, 2); LN1_KSTEP(0, 3);
;     ...
; #pragma unroll
;             for (int eg = 0; eg < 4; ++eg) *(LAS f32x4*)(PL + (wave * 16 + fr) * 64 + eg * 16 + fq * 4) = acc[eg]; }
;         lds_barrier(); tm_seg(F, 20);
.LBB0_1286:
	ds_read_b128 v[164:167], v220
	ds_read_b128 v[168:171], v220 offset:33024
	s_waitcnt vmcnt(24)
	v_readlane_b32 s0, v253, 28
	s_add_i32 s0, s0, s19
	s_waitcnt lgkmcnt(1)
	v_mfma_f32_16x16x32_bf16 v[172:175], v[0:3], v[164:167], 0
	s_cmp_lt_i32 s0, s5
	s_cselect_b64 s[14:15], -1, 0
	s_cmp_ge_i32 s0, s5
	v_mfma_f32_16x16x32_bf16 v[176:179], v[8:11], v[164:167], 0
	v_mfma_f32_16x16x32_bf16 v[182:185], v[16:19], v[164:167], 0
	v_mfma_f32_16x16x32_bf16 v[186:189], v[24:27], v[164:167], 0
	v_mfma_f32_16x16x32_bf16 v[172:175], v[4:7], v[164:167], v[172:175]
	v_mfma_f32_16x16x32_bf16 v[176:179], v[12:15], v[164:167], v[176:179]
	v_mfma_f32_16x16x32_bf16 v[182:185], v[20:23], v[164:167], v[182:185]
	v_mfma_f32_16x16x32_bf16 v[164:167], v[28:31], v[164:167], v[186:189]
	s_waitcnt lgkmcnt(0)
	v_mfma_f32_16x16x32_bf16 v[172:175], v[0:3], v[168:171], v[172:175]
	v_mfma_f32_16x16x32_bf16 v[176:179], v[8:11], v[168:171], v[176:179]
	v_mfma_f32_16x16x32_bf16 v[182:185], v[16:19], v[168:171], v[182:185]
	v_mfma_f32_16x16x32_bf16 v[164:167], v[24:27], v[168:171], v[164:167]
	ds_read_b128 v[168:171], v220 offset:64
	ds_read_b128 v[186:189], v220 offset:33088
	s_waitcnt vmcnt(16)
	s_waitcnt lgkmcnt(1)
	v_mfma_f32_16x16x32_bf16 v[172:175], v[32:35], v[168:171], v[172:175]
	v_mfma_f32_16x16x32_bf16 v[176:179], v[40:43], v[168:171], v[176:179]
	v_mfma_f32_16x16x32_bf16 v[182:185], v[48:51], v[168:171], v[182:185]
	v_mfma_f32_16x16x32_bf16 v[164:167], v[56:59], v[168:171], v[164:167]
	v_mfma_f32_16x16x32_bf16 v[172:175], v[36:39], v[168:171], v[172:175]
	v_mfma_f32_16x16x32_bf16 v[176:179], v[44:47], v[168:171], v[176:179]
	v_mfma_f32_16x16x32_bf16 v[182:185], v[52:55], v[168:171], v[182:185]
	v_mfma_f32_16x16x32_bf16 v[164:167], v[60:63], v[168:171], v[164:167]
	s_waitcnt lgkmcnt(0)
	v_mfma_f32_16x16x32_bf16 v[172:175], v[32:35], v[186:189], v[172:175]
	v_mfma_f32_16x16x32_bf16 v[176:179], v[40:43], v[186:189], v[176:179]
	v_mfma_f32_16x16x32_bf16 v[182:185], v[48:51], v[186:189], v[182:185]
	v_mfma_f32_16x16x32_bf16 v[164:167], v[56:59], v[186:189], v[164:167]
	ds_read_b128 v[168:171], v220 offset:128
	ds_read_b128 v[186:189], v220 offset:33152
	s_waitcnt vmcnt(8)
	s_waitcnt lgkmcnt(1)
	v_mfma_f32_16x16x32_bf16 v[172:175], v[64:67], v[168:171], v[172:175]
	v_mfma_f32_16x16x32_bf16 v[68:71], v[68:71], v[168:171], v[172:175]
	s_waitcnt lgkmcnt(0)
	v_mfma_f32_16x16x32_bf16 v[64:67], v[64:67], v[186:189], v[68:71]
	v_mfma_f32_16x16x32_bf16 v[68:71], v[72:75], v[168:171], v[176:179]
	v_mfma_f32_16x16x32_bf16 v[68:71], v[76:79], v[168:171], v[68:71]
	v_mfma_f32_16x16x32_bf16 v[68:71], v[72:75], v[186:189], v[68:71]
	v_mfma_f32_16x16x32_bf16 v[72:75], v[80:83], v[168:171], v[182:185]
	v_mfma_f32_16x16x32_bf16 v[72:75], v[84:87], v[168:171], v[72:75]
	v_mfma_f32_16x16x32_bf16 v[76:79], v[88:91], v[168:171], v[164:167]
	v_mfma_f32_16x16x32_bf16 v[72:75], v[80:83], v[186:189], v[72:75]
	ds_read_b128 v[80:83], v220 offset:192
	ds_read_b128 v[84:87], v220 offset:33216
	s_waitcnt vmcnt(0)
	v_mfma_f32_16x16x32_bf16 v[76:79], v[92:95], v[168:171], v[76:79]
	v_mfma_f32_16x16x32_bf16 v[76:79], v[88:91], v[186:189], v[76:79]
	s_waitcnt lgkmcnt(1)
	v_mfma_f32_16x16x32_bf16 v[64:67], v[96:99], v[80:83], v[64:67]
	v_mfma_f32_16x16x32_bf16 v[68:71], v[104:107], v[80:83], v[68:71]
	v_mfma_f32_16x16x32_bf16 v[72:75], v[112:115], v[80:83], v[72:75]
	v_mfma_f32_16x16x32_bf16 v[64:67], v[100:103], v[80:83], v[64:67]
	v_mfma_f32_16x16x32_bf16 v[76:79], v[120:123], v[80:83], v[76:79]
	v_mfma_f32_16x16x32_bf16 v[68:71], v[108:111], v[80:83], v[68:71]
	v_mfma_f32_16x16x32_bf16 v[72:75], v[116:119], v[80:83], v[72:75]
	s_waitcnt lgkmcnt(0)
	v_mfma_f32_16x16x32_bf16 v[64:67], v[96:99], v[84:87], v[64:67]
	v_mfma_f32_16x16x32_bf16 v[76:79], v[124:127], v[80:83], v[76:79]
	v_mfma_f32_16x16x32_bf16 v[68:71], v[104:107], v[84:87], v[68:71]
	v_mfma_f32_16x16x32_bf16 v[72:75], v[112:115], v[84:87], v[72:75]
	s_nop 4
	ds_write_b128 v230, v[64:67]
	s_nop 0
	ds_write_b128 v230, v[68:71] offset:64
	ds_write_b128 v230, v[72:75] offset:128
	v_mfma_f32_16x16x32_bf16 v[64:67], v[120:123], v[84:87], v[76:79]
	s_nop 7
	ds_write_b128 v230, v[64:67] offset:192
	s_waitcnt lgkmcnt(0)
	s_barrier
	s_cbranch_scc1 .LBB0_1290
	v_readlane_b32 s0, v254, 17
	s_add_i32 s0, s0, s45
	s_min_i32 s0, s0, 0x8000
	s_ashr_i32 s0, s0, 12
	v_readlane_b32 s1, v254, 58
	s_add_i32 s0, s0, s1
	s_mul_hi_i32 s1, s0, 0x6000
	s_mulk_i32 s0, 0x6000
	s_add_u32 s0, s12, s0
	s_addc_u32 s1, s13, s1
	v_lshl_add_u64 v[64:65], v[130:131], 2, s[0:1]
	s_mov_b64 s[0:1], 0x4000
	v_lshl_add_u64 v[66:67], v[64:65], 0, s[0:1]
	s_mov_b64 s[0:1], 0x3000
	v_lshl_add_u64 v[68:69], v[64:65], 0, s[0:1]
	s_movk_i32 s0, 0x4000
	v_add_co_u32_e32 v70, vcc, s0, v64
	s_movk_i32 s0, 0x3000
	s_nop 0
	v_addc_co_u32_e32 v71, vcc, 0, v65, vcc
	v_add_co_u32_e32 v64, vcc, s0, v64
	v_readlane_b32 s0, v254, 13
	s_nop 0
	v_addc_co_u32_e32 v65, vcc, 0, v65, vcc
	global_load_dwordx4 v[124:127], v[70:71], off
	global_load_dwordx4 v[100:103], v[64:65], off
	ds_read_b128 v[104:107], v150
	ds_read_b128 v[92:95], v150 offset:1024
	ds_read_b128 v[108:111], v150 offset:4096
	ds_read_b128 v[96:99], v150 offset:5120
	global_load_dwordx4 v[120:123], v[66:67], off offset:1024
	global_load_dwordx4 v[116:119], v[66:67], off offset:2048
	global_load_dwordx4 v[88:91], v[68:69], off offset:1024
	global_load_dwordx4 v[112:115], v[66:67], off offset:3072
	global_load_dwordx4 v[76:79], v[68:69], off offset:2048
	s_nop 0
	global_load_dwordx4 v[64:67], v[68:69], off offset:3072
	ds_read_b128 v[80:83], v150 offset:2048
	s_nop 0
	ds_read_b128 v[68:71], v150 offset:3072
	ds_read_b128 v[84:87], v150 offset:6144
	ds_read_b128 v[72:75], v150 offset:7168
	s_add_i32 s0, s0, s19
	s_cmp_ge_i32 s0, s5
	v_mov_b64_e32 v[164:165], v[146:147]
	v_mov_b64_e32 v[166:167], v[144:145]
	v_mov_b64_e32 v[168:169], v[142:143]
	v_mov_b64_e32 v[170:171], v[138:139]
	v_mov_b64_e32 v[172:173], v[140:141]
	v_mov_b64_e32 v[174:175], v[136:137]
	v_mov_b64_e32 v[176:177], v[134:135]
	v_mov_b64_e32 v[178:179], v[132:133]
	s_cbranch_scc1 .Lln1_nopf
	s_add_i32 s0, s17, s45
	s_ashr_i32 s1, s0, 31
	s_lshl_b64 s[2:3], s[0:1], 11
	s_add_i32 s0, s0, 1
	s_ashr_i32 s1, s0, 31
	s_lshl_b64 s[0:1], s[0:1], 11
	v_lshl_add_u64 v[170:171], v[154:155], 0, s[2:3]
	v_lshl_add_u64 v[178:179], v[154:155], 0, s[0:1]
	global_load_dwordx2 v[164:165], v[170:171], off nt
	global_load_dwordx2 v[166:167], v[170:171], off offset:512 nt
	global_load_dwordx2 v[168:169], v[170:171], off offset:1024 nt
	s_nop 0
	global_load_dwordx2 v[170:171], v[170:171], off offset:1536 nt
	s_nop 0
	global_load_dwordx2 v[172:173], v[178:179], off nt
	global_load_dwordx2 v[174:175], v[178:179], off offset:512 nt
	global_load_dwordx2 v[176:177], v[178:179], off offset:1024 nt
	s_nop 0
	global_load_dwordx2 v[178:179], v[178:179], off offset:1536 nt
	s_branch .LBB0_1289

.LBB0_1289:
	v_lshlrev_b32_e32 v203, 16, v147
	v_lshlrev_b32_e32 v202, 16, v146
	v_and_b32_e32 v205, 0xffff0000, v147
	v_and_b32_e32 v204, 0xffff0000, v146
	v_lshlrev_b32_e32 v207, 16, v145
	v_lshlrev_b32_e32 v206, 16, v144
	v_and_b32_e32 v209, 0xffff0000, v145
	v_and_b32_e32 v208, 0xffff0000, v144
	v_pk_add_f32 v[182:183], v[202:203], v[204:205]
	v_lshlrev_b32_e32 v193, 16, v138
	v_and_b32_e32 v189, 0xffff0000, v138
	v_lshlrev_b32_e32 v191, 16, v139
	v_and_b32_e32 v187, 0xffff0000, v139
	v_lshlrev_b32_e32 v138, 16, v134
	v_and_b32_e32 v139, 0xffff0000, v134
	v_add_f32_e32 v134, v182, v183
	v_pk_add_f32 v[182:183], v[206:207], v[208:209]
	v_lshlrev_b32_e32 v198, 16, v142
	v_and_b32_e32 v199, 0xffff0000, v142
	v_lshlrev_b32_e32 v196, 16, v143
	v_and_b32_e32 v197, 0xffff0000, v143
	v_pk_add_f32 v[182:183], v[182:183], v[182:183] op_sel:[0,1] op_sel_hi:[1,0]
	v_add_f32_e32 v192, 0, v134
	v_add_f32_e32 v190, v198, v199
	v_add_f32_e32 v186, v196, v197
	v_mov_b32_e32 v183, v189
	v_pk_add_f32 v[182:183], v[192:193], v[182:183]
	v_pk_add_f32 v[184:185], v[190:191], v[186:187]
	v_mov_b32_e32 v245, 0x3a800000
	v_pk_add_f32 v[182:183], v[182:183], v[184:185]
	s_mov_b32 s46, 0xf800000
	v_add_f32_e32 v134, v182, v183
	v_mov_b32_e32 v182, v181
	v_lshlrev_b32_e32 v147, 16, v141
	v_add_f32_dpp v134, v134, v134 row_shr:1 row_mask:0xf bank_mask:0xf bound_ctrl:1
	v_lshlrev_b32_e32 v146, 16, v140
	v_and_b32_e32 v145, 0xffff0000, v141
	v_add_f32_dpp v134, v134, v134 row_shr:2 row_mask:0xf bank_mask:0xf bound_ctrl:1
	v_and_b32_e32 v144, 0xffff0000, v140
	v_lshlrev_b32_e32 v143, 16, v137
	v_add_f32_dpp v134, v134, v134 row_shr:4 row_mask:0xf bank_mask:0xf bound_ctrl:1
	v_lshlrev_b32_e32 v142, 16, v136
	v_and_b32_e32 v141, 0xffff0000, v137
	v_add_f32_dpp v134, v134, v134 row_shr:8 row_mask:0xf bank_mask:0xf bound_ctrl:1
	v_and_b32_e32 v140, 0xffff0000, v136
	v_lshlrev_b32_e32 v136, 16, v135
	v_mov_b32_dpp v182, v134 row_bcast:15 row_mask:0xa bank_mask:0xf
	v_add_f32_e32 v134, v134, v182
	v_mov_b32_e32 v182, v181
	v_and_b32_e32 v137, 0xffff0000, v135
	v_lshlrev_b32_e32 v135, 16, v132
	v_mov_b32_dpp v182, v134 row_bcast:31 row_mask:0xc bank_mask:0xf
	v_add_f32_e32 v134, v134, v182
	v_lshlrev_b32_e32 v185, 16, v133
	v_readlane_b32 s0, v134, 63
	v_and_b32_e32 v133, 0xffff0000, v133
	s_waitcnt vmcnt(15)
	v_pk_add_f32 v[124:125], v[124:125], 1.0 op_sel_hi:[1,0]
	v_fmac_f32_e32 v205, s0, v217
	v_fmac_f32_e32 v204, s0, v217
	v_fmac_f32_e32 v203, s0, v217
	v_fmac_f32_e32 v202, s0, v217
	v_mul_f32_e32 v134, v204, v204
	v_mul_f32_e32 v182, v205, v205
	v_fmac_f32_e32 v134, v202, v202
	v_fmac_f32_e32 v182, v203, v203
	v_fmac_f32_e32 v209, s0, v217
	v_fmac_f32_e32 v208, s0, v217
	v_add_f32_e32 v134, v134, v182
	v_fmac_f32_e32 v207, s0, v217
	v_fmac_f32_e32 v206, s0, v217
	v_mul_f32_e32 v182, v208, v208
	v_mul_f32_e32 v183, v209, v209
	v_fmac_f32_e32 v182, v206, v206
	v_fmac_f32_e32 v183, v207, v207
	v_add_f32_e32 v182, v182, v183
	v_fmac_f32_e32 v197, s0, v217
	v_fmac_f32_e32 v199, s0, v217
	v_add_f32_e32 v134, v134, v182
	v_fmac_f32_e32 v196, s0, v217
	v_fmac_f32_e32 v198, s0, v217
	v_mul_f32_e32 v182, v199, v199
	v_mul_f32_e32 v183, v197, v197
	v_fmac_f32_e32 v182, v198, v198
	v_fmac_f32_e32 v183, v196, v196
	v_add_f32_e32 v182, v182, v183
	v_fmac_f32_e32 v187, s0, v217
	v_fmac_f32_e32 v189, s0, v217
	v_add_f32_e32 v134, v182, v134
	v_fmac_f32_e32 v191, s0, v217
	v_fmac_f32_e32 v193, s0, v217
	v_mul_f32_e32 v182, v189, v189
	v_mul_f32_e32 v183, v187, v187
	v_fmac_f32_e32 v182, v193, v193
	v_fmac_f32_e32 v183, v191, v191
	v_add_f32_e32 v182, v182, v183
	v_add_f32_e32 v134, v182, v134
	v_mov_b32_e32 v182, v181
	v_and_b32_e32 v183, 0xffff0000, v132
	v_add_f32_dpp v134, v134, v134 row_shr:1 row_mask:0xf bank_mask:0xf bound_ctrl:1
	v_mov_b32_e32 v238, v202
	v_mov_b32_e32 v239, v204
	v_add_f32_dpp v134, v134, v134 row_shr:2 row_mask:0xf bank_mask:0xf bound_ctrl:1
	v_mov_b32_e32 v204, v203
	v_pk_add_f32 v[126:127], v[126:127], 1.0 op_sel_hi:[1,0]
	v_add_f32_dpp v134, v134, v134 row_shr:4 row_mask:0xf bank_mask:0xf bound_ctrl:1
	s_waitcnt vmcnt(13)
	v_pk_add_f32 v[120:121], v[120:121], 1.0 op_sel_hi:[1,0]
	v_pk_add_f32 v[122:123], v[122:123], 1.0 op_sel_hi:[1,0]
	v_add_f32_dpp v134, v134, v134 row_shr:8 row_mask:0xf bank_mask:0xf bound_ctrl:1
	s_waitcnt vmcnt(12)
	v_pk_add_f32 v[116:117], v[116:117], 1.0 op_sel_hi:[1,0]
	v_pk_add_f32 v[118:119], v[118:119], 1.0 op_sel_hi:[1,0]
	v_mov_b32_dpp v182, v134 row_bcast:15 row_mask:0xa bank_mask:0xf
	v_add_f32_e32 v134, v134, v182
	v_mov_b32_e32 v182, v181
	s_waitcnt vmcnt(10)
	v_pk_add_f32 v[112:113], v[112:113], 1.0 op_sel_hi:[1,0]
	v_pk_add_f32 v[114:115], v[114:115], 1.0 op_sel_hi:[1,0]
	v_mov_b32_dpp v182, v134 row_bcast:31 row_mask:0xc bank_mask:0xf
	v_add_f32_e32 v134, v134, v182
	s_nop 0
	v_readlane_b32 s0, v134, 63
	s_nop 1
	v_fma_f32 v134, s0, v245, v242
	v_mul_f32_e32 v182, 0x4f800000, v134
	v_cmp_gt_f32_e32 vcc, s46, v134
	s_nop 1
	v_cndmask_b32_e32 v134, v134, v182, vcc
	v_sqrt_f32_e32 v182, v134
	s_nop 0
	v_add_u32_e32 v132, -1, v182
	v_fma_f32 v184, -v132, v182, v134
	v_cmp_ge_f32_e64 s[40:41], 0, v184
	v_add_u32_e32 v184, 1, v182
	s_nop 0
	v_cndmask_b32_e64 v132, v182, v132, s[40:41]
	v_fma_f32 v182, -v184, v182, v134
	v_cmp_lt_f32_e64 s[40:41], 0, v182
	s_nop 1
	v_cndmask_b32_e64 v132, v132, v184, s[40:41]
	v_mul_f32_e32 v182, 0x37800000, v132
	v_cndmask_b32_e32 v132, v132, v182, vcc
	v_cmp_class_f32_e32 vcc, v134, v243
	s_nop 1
	v_cndmask_b32_e32 v132, v132, v134, vcc
	v_div_scale_f32 v134, s[0:1], v132, v132, 1.0
	v_rcp_f32_e32 v182, v134
	s_add_i32 s0, s18, s45
	s_ashr_i32 s1, s0, 31
	s_lshl_b64 s[2:3], s[0:1], 11
	v_fma_f32 v184, -v134, v182, 1.0
	v_fmac_f32_e32 v182, v184, v182
	v_div_scale_f32 v184, vcc, 1.0, v132, 1.0
	v_mul_f32_e32 v186, v184, v182
	v_fma_f32 v188, -v134, v186, v184
	v_fmac_f32_e32 v186, v188, v182
	v_fma_f32 v134, -v134, v186, v184
	v_div_fmas_f32 v134, v134, v182, v186
	v_div_fixup_f32 v132, v134, v132, 1.0
	v_pk_mul_f32 v[238:239], v[238:239], v[132:133] op_sel_hi:[1,0]
	v_pk_mul_f32 v[202:203], v[204:205], v[132:133] op_sel_hi:[1,0]
	s_waitcnt lgkmcnt(0)
	v_pk_fma_f32 v[204:205], v[104:105], v[238:239], v[108:109]
	v_pk_fma_f32 v[202:203], v[106:107], v[202:203], v[110:111]
	v_cvt_pk_bf16_f32 v238, v204, v205
	v_pk_fma_f32 v[204:205], v[124:125], v[204:205], v[100:101]
	v_mov_b32_e32 v134, v181
	v_lshl_add_u64 v[236:237], v[156:157], 0, s[2:3]
	v_cvt_pk_bf16_f32 v239, v202, v203
	v_cvt_pk_fp8_f32 v134, v204, v205
	global_store_dwordx2 v[236:237], v[238:239], off
	v_pk_fma_f32 v[202:203], v[126:127], v[202:203], v[102:103]
	v_cvt_pk_bf16_f32 v238, v204, v205
	v_cvt_pk_bf16_f32 v239, v202, v203
	v_lshlrev_b32_e32 v240, 16, v238
	v_and_b32_e32 v241, 0xffff0000, v238
	v_pk_add_f32 v[204:205], v[204:205], v[240:241] neg_lo:[0,1] neg_hi:[0,1]
	v_lshlrev_b32_e32 v240, 16, v239
	v_and_b32_e32 v241, 0xffff0000, v239
	v_cvt_pk_fp8_f32 v134, v202, v203 op_sel:[0,0,1]
	v_pk_add_f32 v[202:203], v[202:203], v[240:241] neg_lo:[0,1] neg_hi:[0,1]
	v_cvt_pk_bf16_f32 v204, v204, v205
	v_cvt_pk_bf16_f32 v205, v202, v203
	v_mov_b32_e32 v202, v206
	v_mov_b32_e32 v203, v208
	s_lshl_b64 s[2:3], s[0:1], 10
	v_pk_mul_f32 v[202:203], v[202:203], v[132:133] op_sel_hi:[1,0]
	v_lshl_add_u64 v[194:195], v[158:159], 0, s[2:3]
	v_mov_b32_e32 v208, v207
	v_pk_fma_f32 v[202:203], v[92:93], v[202:203], v[96:97]
	global_store_dword v[194:195], v134, off
	v_pk_mul_f32 v[206:207], v[208:209], v[132:133] op_sel_hi:[1,0]
	v_cvt_pk_bf16_f32 v208, v202, v203
	v_pk_fma_f32 v[202:203], v[120:121], v[202:203], v[88:89]
	v_mov_b32_e32 v134, v181
	v_cvt_pk_fp8_f32 v134, v202, v203
	v_pk_fma_f32 v[206:207], v[94:95], v[206:207], v[98:99]
	v_pk_mul_f32 v[198:199], v[198:199], v[132:133] op_sel_hi:[1,0]
	v_cvt_pk_bf16_f32 v209, v206, v207
	global_store_dwordx2 v[236:237], v[208:209], off offset:512
	v_pk_fma_f32 v[206:207], v[122:123], v[206:207], v[90:91]
	v_cvt_pk_bf16_f32 v208, v202, v203
	v_cvt_pk_bf16_f32 v209, v206, v207
	v_lshlrev_b32_e32 v240, 16, v208
	v_and_b32_e32 v241, 0xffff0000, v208
	v_cvt_pk_fp8_f32 v134, v206, v207 op_sel:[0,0,1]
	v_pk_add_f32 v[202:203], v[202:203], v[240:241] neg_lo:[0,1] neg_hi:[0,1]
	v_lshlrev_b32_e32 v240, 16, v209
	v_and_b32_e32 v241, 0xffff0000, v209
	v_pk_add_f32 v[206:207], v[206:207], v[240:241] neg_lo:[0,1] neg_hi:[0,1]
	v_cvt_pk_bf16_f32 v202, v202, v203
	v_cvt_pk_bf16_f32 v203, v206, v207
	v_add_u32_e32 v182, 0x100, v224
	s_waitcnt vmcnt(12)
	v_pk_fma_f32 v[198:199], v[80:81], v[198:199], v[84:85]
	global_store_dword v[194:195], v134, off offset:256
	ds_write2st64_b64 v182, v[204:205], v[202:203] offset0:64 offset1:65
	v_pk_mul_f32 v[196:197], v[196:197], v[132:133] op_sel_hi:[1,0]
	v_cvt_pk_bf16_f32 v202, v198, v199
	v_pk_fma_f32 v[198:199], v[116:117], v[198:199], v[76:77]
	v_mov_b32_e32 v134, v181
	v_pk_fma_f32 v[196:197], v[82:83], v[196:197], v[86:87]
	v_cvt_pk_fp8_f32 v134, v198, v199
	v_cvt_pk_bf16_f32 v203, v196, v197
	global_store_dwordx2 v[236:237], v[202:203], off offset:1024
	v_pk_fma_f32 v[196:197], v[118:119], v[196:197], v[78:79]
	v_cvt_pk_bf16_f32 v202, v198, v199
	v_mov_b32_e32 v188, v193
	v_cvt_pk_bf16_f32 v203, v196, v197
	v_lshlrev_b32_e32 v204, 16, v202
	v_and_b32_e32 v205, 0xffff0000, v202
	v_pk_mul_f32 v[188:189], v[188:189], v[132:133] op_sel_hi:[1,0]
	v_pk_add_f32 v[198:199], v[198:199], v[204:205] neg_lo:[0,1] neg_hi:[0,1]
	v_lshlrev_b32_e32 v204, 16, v203
	v_cvt_pk_fp8_f32 v134, v196, v197 op_sel:[0,0,1]
	v_and_b32_e32 v205, 0xffff0000, v203
	v_mov_b32_e32 v186, v191
	s_waitcnt vmcnt(13)
	v_pk_fma_f32 v[188:189], v[68:69], v[188:189], v[72:73]
	v_pk_add_f32 v[196:197], v[196:197], v[204:205] neg_lo:[0,1] neg_hi:[0,1]
	v_pk_mul_f32 v[186:187], v[186:187], v[132:133] op_sel_hi:[1,0]
	v_cvt_pk_bf16_f32 v190, v188, v189
	v_pk_fma_f32 v[188:189], v[112:113], v[188:189], v[64:65]
	v_mov_b32_e32 v204, v181
	v_pk_fma_f32 v[186:187], v[70:71], v[186:187], v[74:75]
	v_cvt_pk_fp8_f32 v204, v188, v189
	v_cvt_pk_bf16_f32 v191, v186, v187
	v_pk_fma_f32 v[186:187], v[114:115], v[186:187], v[66:67]
	global_store_dword v[194:195], v134, off offset:512
	global_store_dwordx2 v[236:237], v[190:191], off offset:1536
	v_cvt_pk_bf16_f32 v190, v188, v189
	v_cvt_pk_bf16_f32 v191, v186, v187
	v_cvt_pk_bf16_f32 v198, v198, v199
	v_cvt_pk_bf16_f32 v199, v196, v197
	v_lshlrev_b32_e32 v192, 16, v190
	v_and_b32_e32 v193, 0xffff0000, v190
	v_lshlrev_b32_e32 v196, 16, v191
	v_and_b32_e32 v197, 0xffff0000, v191
	v_pk_add_f32 v[192:193], v[188:189], v[192:193] neg_lo:[0,1] neg_hi:[0,1]
	v_pk_add_f32 v[188:189], v[186:187], v[196:197] neg_lo:[0,1] neg_hi:[0,1]
	v_cvt_pk_fp8_f32 v204, v186, v187 op_sel:[0,0,1]
	v_pk_add_f32 v[186:187], v[146:147], v[144:145]
	v_add_f32_e32 v184, v138, v139
	v_add_f32_e32 v132, v186, v187
	v_pk_add_f32 v[186:187], v[142:143], v[140:141]
	v_add_f32_e32 v134, 0, v132
	v_pk_add_f32 v[186:187], v[186:187], v[186:187] op_sel:[0,1] op_sel_hi:[1,0]
	v_add_f32_e32 v132, v136, v137
	v_mov_b32_e32 v187, v183
	v_cvt_pk_bf16_f32 v192, v192, v193
	v_cvt_pk_bf16_f32 v193, v188, v189
	v_pk_add_f32 v[186:187], v[134:135], v[186:187]
	v_pk_add_f32 v[188:189], v[184:185], v[132:133]
	v_mov_b32_e32 v134, v181
	v_pk_add_f32 v[186:187], v[186:187], v[188:189]
	ds_write2st64_b64 v224, v[238:239], v[208:209] offset1:1
	v_add_f32_e32 v132, v186, v187
	global_store_dword v[194:195], v204, off offset:768
	ds_write2st64_b64 v224, v[202:203], v[190:191] offset0:2 offset1:3
	ds_write2st64_b64 v182, v[198:199], v[192:193] offset0:66 offset1:67
	v_add_f32_dpp v132, v132, v132 row_shr:1 row_mask:0xf bank_mask:0xf bound_ctrl:1
	s_add_i32 s0, s0, 1
	s_nop 0
	v_add_f32_dpp v132, v132, v132 row_shr:2 row_mask:0xf bank_mask:0xf bound_ctrl:1
	s_nop 1
	v_add_f32_dpp v132, v132, v132 row_shr:4 row_mask:0xf bank_mask:0xf bound_ctrl:1
	s_nop 1
	v_add_f32_dpp v132, v132, v132 row_shr:8 row_mask:0xf bank_mask:0xf bound_ctrl:1
	s_nop 1
	v_mov_b32_dpp v134, v132 row_bcast:15 row_mask:0xa bank_mask:0xf
	v_add_f32_e32 v132, v132, v134
	v_mov_b32_e32 v134, v181
	s_nop 1
	v_mov_b32_dpp v134, v132 row_bcast:31 row_mask:0xc bank_mask:0xf
	v_add_f32_e32 v132, v132, v134
	s_nop 0
	v_readlane_b32 s1, v132, 63
	s_nop 1
	v_fmac_f32_e32 v145, s1, v217
	v_fmac_f32_e32 v144, s1, v217
	v_fmac_f32_e32 v147, s1, v217
	v_fmac_f32_e32 v146, s1, v217
	v_mul_f32_e32 v132, v144, v144
	v_mul_f32_e32 v134, v145, v145
	v_fmac_f32_e32 v132, v146, v146
	v_fmac_f32_e32 v134, v147, v147
	v_fmac_f32_e32 v141, s1, v217
	v_fmac_f32_e32 v140, s1, v217
	v_add_f32_e32 v132, v132, v134
	v_fmac_f32_e32 v143, s1, v217
	v_fmac_f32_e32 v142, s1, v217
	v_mul_f32_e32 v134, v140, v140
	v_mul_f32_e32 v184, v141, v141
	v_fmac_f32_e32 v134, v142, v142
	v_fmac_f32_e32 v184, v143, v143
	v_add_f32_e32 v134, v134, v184
	v_fmac_f32_e32 v137, s1, v217
	v_fmac_f32_e32 v139, s1, v217
	v_add_f32_e32 v132, v132, v134
	v_fmac_f32_e32 v136, s1, v217
	v_fmac_f32_e32 v138, s1, v217
	v_mul_f32_e32 v134, v139, v139
	v_mul_f32_e32 v184, v137, v137
	v_fmac_f32_e32 v134, v138, v138
	v_fmac_f32_e32 v184, v136, v136
	v_add_f32_e32 v134, v134, v184
	v_fmac_f32_e32 v133, s1, v217
	v_fmac_f32_e32 v183, s1, v217
	v_add_f32_e32 v132, v134, v132
	v_fmac_f32_e32 v185, s1, v217
	v_fmac_f32_e32 v135, s1, v217
	v_mul_f32_e32 v134, v183, v183
	v_mul_f32_e32 v184, v133, v133
	v_fmac_f32_e32 v134, v135, v135
	v_fmac_f32_e32 v184, v185, v185
	v_add_f32_e32 v134, v134, v184
	v_add_f32_e32 v132, v134, v132
	v_mov_b32_e32 v134, v181
	v_mov_b32_e32 v190, v146
	v_add_f32_dpp v132, v132, v132 row_shr:1 row_mask:0xf bank_mask:0xf bound_ctrl:1
	v_mov_b32_e32 v191, v144
	v_mov_b32_e32 v144, v147
	v_add_f32_dpp v132, v132, v132 row_shr:2 row_mask:0xf bank_mask:0xf bound_ctrl:1
	s_waitcnt vmcnt(15)
	v_mov_b64_e32 v[146:147], v[164:165]
	s_nop 0
	v_add_f32_dpp v132, v132, v132 row_shr:4 row_mask:0xf bank_mask:0xf bound_ctrl:1
	s_nop 1
	v_add_f32_dpp v132, v132, v132 row_shr:8 row_mask:0xf bank_mask:0xf bound_ctrl:1
	s_nop 1
	v_mov_b32_dpp v134, v132 row_bcast:15 row_mask:0xa bank_mask:0xf
	v_add_f32_e32 v132, v132, v134
	v_mov_b32_e32 v134, v181
	s_nop 1
	v_mov_b32_dpp v134, v132 row_bcast:31 row_mask:0xc bank_mask:0xf
	v_add_f32_e32 v132, v132, v134
	s_nop 0
	v_readlane_b32 s1, v132, 63
	s_nop 1
	v_fma_f32 v132, s1, v245, v242
	v_mul_f32_e32 v134, 0x4f800000, v132
	v_cmp_gt_f32_e32 vcc, s46, v132
	s_ashr_i32 s1, s0, 31
	s_nop 0
	v_cndmask_b32_e32 v132, v132, v134, vcc
	v_sqrt_f32_e32 v134, v132
	s_nop 0
	v_add_u32_e32 v182, -1, v134
	v_fma_f32 v184, -v182, v134, v132
	v_cmp_ge_f32_e64 s[40:41], 0, v184
	v_add_u32_e32 v184, 1, v134
	s_nop 0
	v_cndmask_b32_e64 v182, v134, v182, s[40:41]
	v_fma_f32 v134, -v184, v134, v132
	v_cmp_lt_f32_e64 s[40:41], 0, v134
	s_nop 1
	v_cndmask_b32_e64 v134, v182, v184, s[40:41]
	v_mul_f32_e32 v182, 0x37800000, v134
	v_cndmask_b32_e32 v134, v134, v182, vcc
	v_cmp_class_f32_e32 vcc, v132, v243
	s_nop 1
	v_cndmask_b32_e32 v132, v134, v132, vcc
	v_div_scale_f32 v134, s[2:3], v132, v132, 1.0
	v_rcp_f32_e32 v182, v134
	s_lshl_b64 s[2:3], s[0:1], 11
	s_lshl_b64 s[0:1], s[0:1], 10
	v_lshl_add_u64 v[188:189], v[158:159], 0, s[0:1]
	v_fma_f32 v184, -v134, v182, 1.0
	v_fmac_f32_e32 v182, v184, v182
	v_div_scale_f32 v184, vcc, 1.0, v132, 1.0
	v_mul_f32_e32 v186, v184, v182
	v_fma_f32 v187, -v134, v186, v184
	v_fmac_f32_e32 v186, v187, v182
	v_fma_f32 v134, -v134, v186, v184
	v_div_fmas_f32 v134, v134, v182, v186
	v_div_fixup_f32 v134, v134, v132, 1.0
	v_pk_mul_f32 v[190:191], v[190:191], v[134:135] op_sel_hi:[1,0]
	v_pk_mul_f32 v[144:145], v[144:145], v[134:135] op_sel_hi:[1,0]
	v_pk_fma_f32 v[104:105], v[104:105], v[190:191], v[108:109]
	v_pk_fma_f32 v[106:107], v[106:107], v[144:145], v[110:111]
	v_lshl_add_u64 v[186:187], v[156:157], 0, s[2:3]
	v_cvt_pk_bf16_f32 v108, v104, v105
	v_cvt_pk_bf16_f32 v109, v106, v107
	global_store_dwordx2 v[186:187], v[108:109], off
	v_pk_fma_f32 v[100:101], v[124:125], v[104:105], v[100:101]
	v_mov_b32_e32 v108, v181
	v_cvt_pk_fp8_f32 v108, v100, v101
	v_pk_fma_f32 v[102:103], v[126:127], v[106:107], v[102:103]
	v_cvt_pk_bf16_f32 v104, v100, v101
	v_cvt_pk_bf16_f32 v105, v102, v103
	v_lshlrev_b32_e32 v106, 16, v104
	v_and_b32_e32 v107, 0xffff0000, v104
	v_pk_add_f32 v[100:101], v[100:101], v[106:107] neg_lo:[0,1] neg_hi:[0,1]
	v_lshlrev_b32_e32 v106, 16, v105
	v_and_b32_e32 v107, 0xffff0000, v105
	v_cvt_pk_fp8_f32 v108, v102, v103 op_sel:[0,0,1]
	v_pk_add_f32 v[102:103], v[102:103], v[106:107] neg_lo:[0,1] neg_hi:[0,1]
	v_cvt_pk_bf16_f32 v100, v100, v101
	v_cvt_pk_bf16_f32 v101, v102, v103
	v_mov_b32_e32 v102, v142
	v_mov_b32_e32 v103, v140
	v_mov_b32_e32 v140, v143
	v_pk_mul_f32 v[102:103], v[102:103], v[134:135] op_sel_hi:[1,0]
	v_pk_mul_f32 v[106:107], v[140:141], v[134:135] op_sel_hi:[1,0]
	v_pk_fma_f32 v[92:93], v[92:93], v[102:103], v[96:97]
	v_pk_fma_f32 v[94:95], v[94:95], v[106:107], v[98:99]
	v_cvt_pk_bf16_f32 v96, v92, v93
	v_cvt_pk_bf16_f32 v97, v94, v95
	global_store_dword v[188:189], v108, off
	global_store_dwordx2 v[186:187], v[96:97], off offset:512
	v_pk_fma_f32 v[88:89], v[120:121], v[92:93], v[88:89]
	v_mov_b32_e32 v96, v181
	v_cvt_pk_fp8_f32 v96, v88, v89
	v_pk_fma_f32 v[90:91], v[122:123], v[94:95], v[90:91]
	v_cvt_pk_bf16_f32 v92, v88, v89
	v_cvt_pk_bf16_f32 v93, v90, v91
	v_lshlrev_b32_e32 v94, 16, v92
	v_and_b32_e32 v95, 0xffff0000, v92
	v_pk_add_f32 v[88:89], v[88:89], v[94:95] neg_lo:[0,1] neg_hi:[0,1]
	v_lshlrev_b32_e32 v94, 16, v93
	v_and_b32_e32 v95, 0xffff0000, v93
	v_cvt_pk_fp8_f32 v96, v90, v91 op_sel:[0,0,1]
	v_pk_add_f32 v[90:91], v[90:91], v[94:95] neg_lo:[0,1] neg_hi:[0,1]
	v_cvt_pk_bf16_f32 v88, v88, v89
	v_cvt_pk_bf16_f32 v89, v90, v91
	ds_write2st64_b64 v225, v[104:105], v[92:93] offset1:1
	v_add_u32_e32 v92, 0x100, v225
	ds_write2st64_b64 v92, v[100:101], v[88:89] offset0:64 offset1:65
	v_pk_mul_f32 v[88:89], v[138:139], v[134:135] op_sel_hi:[1,0]
	v_pk_mul_f32 v[90:91], v[136:137], v[134:135] op_sel_hi:[1,0]
	v_pk_fma_f32 v[80:81], v[80:81], v[88:89], v[84:85]
	v_pk_fma_f32 v[82:83], v[82:83], v[90:91], v[86:87]
	v_cvt_pk_bf16_f32 v84, v80, v81
	v_cvt_pk_bf16_f32 v85, v82, v83
	global_store_dword v[188:189], v96, off offset:256
	global_store_dwordx2 v[186:187], v[84:85], off offset:1024
	v_pk_fma_f32 v[76:77], v[116:117], v[80:81], v[76:77]
	v_mov_b32_e32 v84, v181
	v_cvt_pk_fp8_f32 v84, v76, v77
	v_pk_fma_f32 v[78:79], v[118:119], v[82:83], v[78:79]
	v_cvt_pk_bf16_f32 v80, v76, v77
	v_cvt_pk_bf16_f32 v81, v78, v79
	v_lshlrev_b32_e32 v82, 16, v80
	v_and_b32_e32 v83, 0xffff0000, v80
	v_pk_add_f32 v[76:77], v[76:77], v[82:83] neg_lo:[0,1] neg_hi:[0,1]
	v_lshlrev_b32_e32 v82, 16, v81
	v_and_b32_e32 v83, 0xffff0000, v81
	v_cvt_pk_fp8_f32 v84, v78, v79 op_sel:[0,0,1]
	v_pk_add_f32 v[78:79], v[78:79], v[82:83] neg_lo:[0,1] neg_hi:[0,1]
	v_mov_b32_e32 v182, v135
	v_mov_b32_e32 v132, v185
	v_cvt_pk_bf16_f32 v76, v76, v77
	v_cvt_pk_bf16_f32 v77, v78, v79
	v_pk_mul_f32 v[78:79], v[182:183], v[134:135] op_sel_hi:[1,0]
	v_pk_mul_f32 v[82:83], v[132:133], v[134:135] op_sel_hi:[1,0]
	v_pk_fma_f32 v[68:69], v[68:69], v[78:79], v[72:73]
	v_pk_fma_f32 v[70:71], v[70:71], v[82:83], v[74:75]
	v_cvt_pk_bf16_f32 v72, v68, v69
	v_cvt_pk_bf16_f32 v73, v70, v71
	global_store_dword v[188:189], v84, off offset:512
	global_store_dwordx2 v[186:187], v[72:73], off offset:1536
	v_pk_fma_f32 v[64:65], v[112:113], v[68:69], v[64:65]
	v_mov_b32_e32 v72, v181
	v_cvt_pk_fp8_f32 v72, v64, v65
	v_pk_fma_f32 v[66:67], v[114:115], v[70:71], v[66:67]
	v_cvt_pk_bf16_f32 v68, v64, v65
	v_cvt_pk_bf16_f32 v69, v66, v67
	v_cvt_pk_fp8_f32 v72, v66, v67 op_sel:[0,0,1]
	v_lshlrev_b32_e32 v70, 16, v68
	v_and_b32_e32 v71, 0xffff0000, v68
	v_pk_add_f32 v[64:65], v[64:65], v[70:71] neg_lo:[0,1] neg_hi:[0,1]
	v_lshlrev_b32_e32 v70, 16, v69
	v_and_b32_e32 v71, 0xffff0000, v69
	v_pk_add_f32 v[66:67], v[66:67], v[70:71] neg_lo:[0,1] neg_hi:[0,1]
	s_waitcnt vmcnt(15)
	v_mov_b64_e32 v[132:133], v[178:179]
	v_mov_b64_e32 v[134:135], v[176:177]
	v_mov_b64_e32 v[136:137], v[174:175]
	v_mov_b64_e32 v[140:141], v[172:173]
	v_mov_b64_e32 v[138:139], v[170:171]
	v_mov_b64_e32 v[142:143], v[168:169]
	v_mov_b64_e32 v[144:145], v[166:167]
	v_cvt_pk_bf16_f32 v64, v64, v65
	v_cvt_pk_bf16_f32 v65, v66, v67
	global_store_dword v[188:189], v72, off offset:768
	ds_write2st64_b64 v225, v[80:81], v[68:69] offset0:2 offset1:3
	ds_write2st64_b64 v92, v[76:77], v[64:65] offset0:66 offset1:67

; #define LAS __attribute__((address_space(3)))
; __device__ __forceinline__ void lds_barrier() { asm volatile("s_waitcnt lgkmcnt(0)" ::: "memory"); __builtin_amdgcn_s_barrier(); asm volatile("" ::: "memory"); }
; __device__ __forceinline__ void phase_ln1(Frame& F0, const Args& A, int l, bool v_from_h) {
;     ...
;         lds_barrier(); tm_seg(F, 23);
;         if (g + F.G < ngroups) { LN1_GLDK(0); LN1_GLDK(1); }
;         {
;             float score[2]; unsigned key[2]; int rank[2] = {0, 0};
; #pragma unroll
;             for (int rr = 0; rr < 2; ++rr) { score[rr] = __builtin_amdgcn_rcpf(1.0f + __expf(-LOG[(2 * wave + rr) * 64 + lane]));
;                 key[rr] = (__float_as_uint(score[rr] + brl + 2.0f) & ~63u) | (unsigned)(63 - lane);
;                 KEYS[(2 * wave + rr) * 64 + lane] = key[rr]; }
; #pragma unroll
;             for (int i = 0; i < 16; ++i) {
; #pragma unroll
;                 for (int rr = 0; rr < 2; ++rr) { const v4u kq = *(const LAS v4u*)(KEYS + (2 * wave + rr) * 64 + 4 * i);
;                     rank[rr] += (int)(kq.x > key[rr]) + (int)(kq.y > key[rr]) + (int)(kq.z > key[rr]) + (int)(kq.w > key[rr]); } }
.LBB0_1296:
	s_waitcnt lgkmcnt(0)
	s_barrier
	s_andn2_b64 vcc, exec, s[14:15]
	s_cbranch_vccnz .LBB0_1298
	s_nop 4
	global_load_dwordx4 v[64:67], v219, s[20:21] offset:0x80
	global_load_dwordx4 v[68:71], v219, s[24:25] offset:0x80
	global_load_dwordx4 v[72:75], v219, s[26:27] offset:0x80
	global_load_dwordx4 v[76:79], v219, s[42:43] offset:0x80
	global_load_dwordx4 v[80:83], v219, s[50:51] offset:0x80
	global_load_dwordx4 v[84:87], v219, s[62:63] offset:0x80
	global_load_dwordx4 v[88:91], v219, s[68:69] offset:0x80
	global_load_dwordx4 v[92:95], v219, s[74:75] offset:0x80
	s_nop 4
	global_load_dwordx4 v[96:99], v219, s[20:21] offset:0xc0
	global_load_dwordx4 v[100:103], v219, s[24:25] offset:0xc0
	global_load_dwordx4 v[104:107], v219, s[26:27] offset:0xc0
	global_load_dwordx4 v[108:111], v219, s[42:43] offset:0xc0
	global_load_dwordx4 v[112:115], v219, s[50:51] offset:0xc0
	global_load_dwordx4 v[116:119], v219, s[62:63] offset:0xc0
	global_load_dwordx4 v[120:123], v219, s[68:69] offset:0xc0
	global_load_dwordx4 v[124:127], v219, s[74:75] offset:0xc0
.LBB0_1298:
	ds_read_b32 v166, v226
	ds_read_b32 v167, v228
	v_mov_b32_e32 v171, s44
	v_mov_b32_e32 v180, -1
	s_waitcnt lgkmcnt(1)
	v_mul_f32_e32 v166, 0xbfb8aa3b, v166
	s_waitcnt lgkmcnt(0)
	v_mul_f32_e32 v167, 0xbfb8aa3b, v167
	v_exp_f32_e32 v166, v166
	v_exp_f32_e32 v167, v167
	v_add_f32_e32 v166, 1.0, v166
	v_add_f32_e32 v167, 1.0, v167
	v_rcp_f32_e32 v165, v166
	v_rcp_f32_e32 v164, v167
	s_nop 0
	v_pk_add_f32 v[166:167], v[148:149], v[164:165]
	s_nop 0
	v_pk_add_f32 v[166:167], v[166:167], 2.0 op_sel_hi:[1,0]
	s_nop 0
	v_and_b32_e32 v167, 0xffffffc0, v167
	v_and_b32_e32 v166, 0xffffffc0, v166
	v_or_b32_e32 v170, v167, v129
	v_or_b32_e32 v163, v166, v160
	ds_write_b32 v227, v170
	ds_write_b32 v229, v163
	ds_read_b128 v[172:175], v171
	ds_read_b128 v[176:179], v171 offset:256
	ds_read_b128 v[182:185], v171 offset:16
	ds_read_b128 v[186:189], v171 offset:272
	ds_read_b128 v[190:193], v171 offset:32
	ds_read_b128 v[194:197], v171 offset:288
	ds_read_b128 v[202:205], v171 offset:48
	ds_read_b128 v[206:209], v171 offset:304
	v_mov_b32_e32 v168, 0
	v_mov_b32_e32 v169, 0
	s_waitcnt lgkmcnt(6)
	v_cmp_gt_u32_e32 vcc, v172, v170
	v_cmp_gt_u32_e64 s[40:41], v176, v163
	v_cmp_gt_u32_e64 s[46:47], v173, v170
	v_addc_co_u32_e32 v168, vcc, 0, v168, vcc
	v_addc_co_u32_e64 v169, s[40:41], 0, v169, s[40:41]
	v_addc_co_u32_e64 v168, s[46:47], 0, v168, s[46:47]
	v_cmp_gt_u32_e32 vcc, v177, v163
	v_cmp_gt_u32_e64 s[40:41], v174, v170
	v_cmp_gt_u32_e64 s[46:47], v178, v163
	v_addc_co_u32_e32 v169, vcc, 0, v169, vcc
	v_addc_co_u32_e64 v168, s[40:41], 0, v168, s[40:41]
	v_addc_co_u32_e64 v169, s[46:47], 0, v169, s[46:47]
	s_waitcnt lgkmcnt(4)
	v_cmp_gt_u32_e32 vcc, v175, v170
	v_cmp_gt_u32_e64 s[40:41], v179, v163
	v_cmp_gt_u32_e64 s[46:47], v182, v170
	v_addc_co_u32_e32 v168, vcc, 0, v168, vcc
	v_addc_co_u32_e64 v169, s[40:41], 0, v169, s[40:41]
	v_addc_co_u32_e64 v168, s[46:47], 0, v168, s[46:47]
	ds_read_b128 v[172:175], v171 offset:64
	ds_read_b128 v[176:179], v171 offset:320
	v_cmp_gt_u32_e32 vcc, v186, v163
	v_cmp_gt_u32_e64 s[40:41], v183, v170
	v_cmp_gt_u32_e64 s[46:47], v187, v163
	v_addc_co_u32_e32 v169, vcc, 0, v169, vcc
	v_addc_co_u32_e64 v168, s[40:41], 0, v168, s[40:41]
	v_addc_co_u32_e64 v169, s[46:47], 0, v169, s[46:47]
	v_cmp_gt_u32_e32 vcc, v184, v170
	v_cmp_gt_u32_e64 s[40:41], v188, v163
	v_cmp_gt_u32_e64 s[46:47], v185, v170
	v_addc_co_u32_e32 v168, vcc, 0, v168, vcc
	v_addc_co_u32_e64 v169, s[40:41], 0, v169, s[40:41]
	v_addc_co_u32_e64 v168, s[46:47], 0, v168, s[46:47]
	s_waitcnt lgkmcnt(4)
	v_cmp_gt_u32_e32 vcc, v189, v163
	v_cmp_gt_u32_e64 s[40:41], v190, v170
	v_cmp_gt_u32_e64 s[46:47], v194, v163
	v_addc_co_u32_e32 v169, vcc, 0, v169, vcc
	v_addc_co_u32_e64 v168, s[40:41], 0, v168, s[40:41]
	v_addc_co_u32_e64 v169, s[46:47], 0, v169, s[46:47]
	ds_read_b128 v[182:185], v171 offset:80
	ds_read_b128 v[186:189], v171 offset:336
	v_cmp_gt_u32_e32 vcc, v191, v170
	v_cmp_gt_u32_e64 s[40:41], v195, v163
	v_cmp_gt_u32_e64 s[46:47], v192, v170
	v_addc_co_u32_e32 v168, vcc, 0, v168, vcc
	v_addc_co_u32_e64 v169, s[40:41], 0, v169, s[40:41]
	v_addc_co_u32_e64 v168, s[46:47], 0, v168, s[46:47]
	v_cmp_gt_u32_e32 vcc, v196, v163
	v_cmp_gt_u32_e64 s[40:41], v193, v170
	v_cmp_gt_u32_e64 s[46:47], v197, v163
	v_addc_co_u32_e32 v169, vcc, 0, v169, vcc
	v_addc_co_u32_e64 v168, s[40:41], 0, v168, s[40:41]
	v_addc_co_u32_e64 v169, s[46:47], 0, v169, s[46:47]
	ds_read_b128 v[190:193], v171 offset:96
	ds_read_b128 v[194:197], v171 offset:352
	s_waitcnt lgkmcnt(6)
	v_cmp_gt_u32_e32 vcc, v202, v170
	v_cmp_gt_u32_e64 s[40:41], v206, v163
	v_cmp_gt_u32_e64 s[46:47], v203, v170
	v_addc_co_u32_e32 v168, vcc, 0, v168, vcc
	v_addc_co_u32_e64 v169, s[40:41], 0, v169, s[40:41]
	v_addc_co_u32_e64 v168, s[46:47], 0, v168, s[46:47]
	v_cmp_gt_u32_e32 vcc, v207, v163
	v_cmp_gt_u32_e64 s[40:41], v204, v170
	v_cmp_gt_u32_e64 s[46:47], v208, v163
	v_addc_co_u32_e32 v169, vcc, 0, v169, vcc
	v_addc_co_u32_e64 v168, s[40:41], 0, v168, s[40:41]
	v_addc_co_u32_e64 v169, s[46:47], 0, v169, s[46:47]
	s_waitcnt lgkmcnt(4)
	v_cmp_gt_u32_e32 vcc, v205, v170
	v_cmp_gt_u32_e64 s[40:41], v209, v163
	v_cmp_gt_u32_e64 s[46:47], v172, v170
	v_addc_co_u32_e32 v168, vcc, 0, v168, vcc
	v_addc_co_u32_e64 v169, s[40:41], 0, v169, s[40:41]
	v_addc_co_u32_e64 v168, s[46:47], 0, v168, s[46:47]
	ds_read_b128 v[202:205], v171 offset:112
	ds_read_b128 v[206:209], v171 offset:368
	v_cmp_gt_u32_e32 vcc, v176, v163
	v_cmp_gt_u32_e64 s[40:41], v173, v170
	v_cmp_gt_u32_e64 s[46:47], v177, v163
	v_addc_co_u32_e32 v169, vcc, 0, v169, vcc
	v_addc_co_u32_e64 v168, s[40:41], 0, v168, s[40:41]
	v_addc_co_u32_e64 v169, s[46:47], 0, v169, s[46:47]
	v_cmp_gt_u32_e32 vcc, v174, v170
	v_cmp_gt_u32_e64 s[40:41], v178, v163
	v_cmp_gt_u32_e64 s[46:47], v175, v170
	v_addc_co_u32_e32 v168, vcc, 0, v168, vcc
	v_addc_co_u32_e64 v169, s[40:41], 0, v169, s[40:41]
	v_addc_co_u32_e64 v168, s[46:47], 0, v168, s[46:47]
	s_waitcnt lgkmcnt(4)
; #define LAS __attribute__((address_space(3)))
; __device__ __forceinline__ void phase_ln1(Frame& F0, const Args& A, int l, bool v_from_h) {
;     ...
;             for (int i = 0; i < 16; ++i) {
; #pragma unroll
;                 for (int rr = 0; rr < 2; ++rr) { const v4u kq = *(const LAS v4u*)(KEYS + (2 * wave + rr) * 64 + 4 * i);
;                     rank[rr] += (int)(kq.x > key[rr]) + (int)(kq.y > key[rr]) + (int)(kq.z > key[rr]) + (int)(kq.w > key[rr]); } }
	v_cmp_gt_u32_e32 vcc, v179, v163
	v_cmp_gt_u32_e64 s[40:41], v182, v170
	v_cmp_gt_u32_e64 s[46:47], v186, v163
	v_addc_co_u32_e32 v169, vcc, 0, v169, vcc
	v_addc_co_u32_e64 v168, s[40:41], 0, v168, s[40:41]
	v_addc_co_u32_e64 v169, s[46:47], 0, v169, s[46:47]
	ds_read_b128 v[172:175], v171 offset:128
	ds_read_b128 v[176:179], v171 offset:384
	v_cmp_gt_u32_e32 vcc, v183, v170
	v_cmp_gt_u32_e64 s[40:41], v187, v163
	v_cmp_gt_u32_e64 s[46:47], v184, v170
	v_addc_co_u32_e32 v168, vcc, 0, v168, vcc
	v_addc_co_u32_e64 v169, s[40:41], 0, v169, s[40:41]
	v_addc_co_u32_e64 v168, s[46:47], 0, v168, s[46:47]
	v_cmp_gt_u32_e32 vcc, v188, v163
	v_cmp_gt_u32_e64 s[40:41], v185, v170
	v_cmp_gt_u32_e64 s[46:47], v189, v163
	v_addc_co_u32_e32 v169, vcc, 0, v169, vcc
	v_addc_co_u32_e64 v168, s[40:41], 0, v168, s[40:41]
	v_addc_co_u32_e64 v169, s[46:47], 0, v169, s[46:47]
	ds_read_b128 v[182:185], v171 offset:144
	ds_read_b128 v[186:189], v171 offset:400
	s_waitcnt lgkmcnt(6)
	v_cmp_gt_u32_e32 vcc, v190, v170
	v_cmp_gt_u32_e64 s[40:41], v194, v163
	v_cmp_gt_u32_e64 s[46:47], v191, v170
	v_addc_co_u32_e32 v168, vcc, 0, v168, vcc
	v_addc_co_u32_e64 v169, s[40:41], 0, v169, s[40:41]
	v_addc_co_u32_e64 v168, s[46:47], 0, v168, s[46:47]
	v_cmp_gt_u32_e32 vcc, v195, v163
	v_cmp_gt_u32_e64 s[40:41], v192, v170
	v_cmp_gt_u32_e64 s[46:47], v196, v163
	v_addc_co_u32_e32 v169, vcc, 0, v169, vcc
	v_addc_co_u32_e64 v168, s[40:41], 0, v168, s[40:41]
	v_addc_co_u32_e64 v169, s[46:47], 0, v169, s[46:47]
	s_waitcnt lgkmcnt(4)
	v_cmp_gt_u32_e32 vcc, v193, v170
	v_cmp_gt_u32_e64 s[40:41], v197, v163
	v_cmp_gt_u32_e64 s[46:47], v202, v170
	v_addc_co_u32_e32 v168, vcc, 0, v168, vcc
	v_addc_co_u32_e64 v169, s[40:41], 0, v169, s[40:41]
	v_addc_co_u32_e64 v168, s[46:47], 0, v168, s[46:47]
	ds_read_b128 v[190:193], v171 offset:160
	ds_read_b128 v[194:197], v171 offset:416
	v_cmp_gt_u32_e32 vcc, v206, v163
	v_cmp_gt_u32_e64 s[40:41], v203, v170
	v_cmp_gt_u32_e64 s[46:47], v207, v163
	v_addc_co_u32_e32 v169, vcc, 0, v169, vcc
	v_addc_co_u32_e64 v168, s[40:41], 0, v168, s[40:41]
	v_addc_co_u32_e64 v169, s[46:47], 0, v169, s[46:47]
	v_cmp_gt_u32_e32 vcc, v204, v170
	v_cmp_gt_u32_e64 s[40:41], v208, v163
	v_cmp_gt_u32_e64 s[46:47], v205, v170
	v_addc_co_u32_e32 v168, vcc, 0, v168, vcc
	v_addc_co_u32_e64 v169, s[40:41], 0, v169, s[40:41]
	v_addc_co_u32_e64 v168, s[46:47], 0, v168, s[46:47]
	s_waitcnt lgkmcnt(4)
	v_cmp_gt_u32_e32 vcc, v209, v163
	v_cmp_gt_u32_e64 s[40:41], v172, v170
	v_cmp_gt_u32_e64 s[46:47], v176, v163
	v_addc_co_u32_e32 v169, vcc, 0, v169, vcc
	v_addc_co_u32_e64 v168, s[40:41], 0, v168, s[40:41]
	v_addc_co_u32_e64 v169, s[46:47], 0, v169, s[46:47]
	ds_read_b128 v[202:205], v171 offset:176
	ds_read_b128 v[206:209], v171 offset:432
	v_cmp_gt_u32_e32 vcc, v173, v170
	v_cmp_gt_u32_e64 s[40:41], v177, v163
	v_cmp_gt_u32_e64 s[46:47], v174, v170
	v_addc_co_u32_e32 v168, vcc, 0, v168, vcc
	v_addc_co_u32_e64 v169, s[40:41], 0, v169, s[40:41]
	v_addc_co_u32_e64 v168, s[46:47], 0, v168, s[46:47]
	v_cmp_gt_u32_e32 vcc, v178, v163
	v_cmp_gt_u32_e64 s[40:41], v175, v170
	v_cmp_gt_u32_e64 s[46:47], v179, v163
	v_addc_co_u32_e32 v169, vcc, 0, v169, vcc
	v_addc_co_u32_e64 v168, s[40:41], 0, v168, s[40:41]
	v_addc_co_u32_e64 v169, s[46:47], 0, v169, s[46:47]
	ds_read_b128 v[172:175], v171 offset:192
	ds_read_b128 v[176:179], v171 offset:448
	s_waitcnt lgkmcnt(6)
	v_cmp_gt_u32_e32 vcc, v182, v170
	v_cmp_gt_u32_e64 s[40:41], v186, v163
	v_cmp_gt_u32_e64 s[46:47], v183, v170
	v_addc_co_u32_e32 v168, vcc, 0, v168, vcc
	v_addc_co_u32_e64 v169, s[40:41], 0, v169, s[40:41]
	v_addc_co_u32_e64 v168, s[46:47], 0, v168, s[46:47]
	v_cmp_gt_u32_e32 vcc, v187, v163
	v_cmp_gt_u32_e64 s[40:41], v184, v170
	v_cmp_gt_u32_e64 s[46:47], v188, v163
	v_addc_co_u32_e32 v169, vcc, 0, v169, vcc
	v_addc_co_u32_e64 v168, s[40:41], 0, v168, s[40:41]
	v_addc_co_u32_e64 v169, s[46:47], 0, v169, s[46:47]
	s_waitcnt lgkmcnt(4)
	v_cmp_gt_u32_e32 vcc, v185, v170
	v_cmp_gt_u32_e64 s[40:41], v189, v163
	v_cmp_gt_u32_e64 s[46:47], v190, v170
	v_addc_co_u32_e32 v168, vcc, 0, v168, vcc
	v_addc_co_u32_e64 v169, s[40:41], 0, v169, s[40:41]
	v_addc_co_u32_e64 v168, s[46:47], 0, v168, s[46:47]
	ds_read_b128 v[182:185], v171 offset:208
	ds_read_b128 v[186:189], v171 offset:464
	v_cmp_gt_u32_e32 vcc, v194, v163
	v_cmp_gt_u32_e64 s[40:41], v191, v170
	v_cmp_gt_u32_e64 s[46:47], v195, v163
	v_addc_co_u32_e32 v169, vcc, 0, v169, vcc
	v_addc_co_u32_e64 v168, s[40:41], 0, v168, s[40:41]
	v_addc_co_u32_e64 v169, s[46:47], 0, v169, s[46:47]
	v_cmp_gt_u32_e32 vcc, v192, v170
	v_cmp_gt_u32_e64 s[40:41], v196, v163
	v_cmp_gt_u32_e64 s[46:47], v193, v170
	v_addc_co_u32_e32 v168, vcc, 0, v168, vcc
	v_addc_co_u32_e64 v169, s[40:41], 0, v169, s[40:41]
	v_addc_co_u32_e64 v168, s[46:47], 0, v168, s[46:47]
	s_waitcnt lgkmcnt(4)
; #define LAS __attribute__((address_space(3)))
; __device__ __forceinline__ void phase_ln1(Frame& F0, const Args& A, int l, bool v_from_h) {
;     ...
;             for (int i = 0; i < 16; ++i) {
; #pragma unroll
;                 for (int rr = 0; rr < 2; ++rr) { const v4u kq = *(const LAS v4u*)(KEYS + (2 * wave + rr) * 64 + 4 * i);
;                     rank[rr] += (int)(kq.x > key[rr]) + (int)(kq.y > key[rr]) + (int)(kq.z > key[rr]) + (int)(kq.w > key[rr]); } }
; #pragma unroll
;             for (int rr = 0; rr < 2; ++rr) { const bool sel = rank[rr] < 8; const float ssum = wave_sum(sel ? score[rr] : 0.f);
;                 pend_r[rr] = sel ? rank[rr] : -1; pend_w[rr] = score[rr] / ssum * ROUTED_SCALE; if (sel) atomicAdd((int*)&lhist[lane], 1); }
	v_cmp_gt_u32_e32 vcc, v197, v163
	v_cmp_gt_u32_e64 s[40:41], v202, v170
	v_cmp_gt_u32_e64 s[46:47], v206, v163
	v_addc_co_u32_e32 v169, vcc, 0, v169, vcc
	v_addc_co_u32_e64 v168, s[40:41], 0, v168, s[40:41]
	v_addc_co_u32_e64 v169, s[46:47], 0, v169, s[46:47]
	ds_read_b128 v[190:193], v171 offset:224
	ds_read_b128 v[194:197], v171 offset:480
	v_cmp_gt_u32_e32 vcc, v203, v170
	v_cmp_gt_u32_e64 s[40:41], v207, v163
	v_cmp_gt_u32_e64 s[46:47], v204, v170
	v_addc_co_u32_e32 v168, vcc, 0, v168, vcc
	v_addc_co_u32_e64 v169, s[40:41], 0, v169, s[40:41]
	v_addc_co_u32_e64 v168, s[46:47], 0, v168, s[46:47]
	v_cmp_gt_u32_e32 vcc, v208, v163
	v_cmp_gt_u32_e64 s[40:41], v205, v170
	v_cmp_gt_u32_e64 s[46:47], v209, v163
	v_addc_co_u32_e32 v169, vcc, 0, v169, vcc
	v_addc_co_u32_e64 v168, s[40:41], 0, v168, s[40:41]
	v_addc_co_u32_e64 v169, s[46:47], 0, v169, s[46:47]
	ds_read_b128 v[202:205], v171 offset:240
	ds_read_b128 v[206:209], v171 offset:496
	s_waitcnt lgkmcnt(6)
	v_cmp_gt_u32_e32 vcc, v172, v170
	v_cmp_gt_u32_e64 s[40:41], v176, v163
	v_cmp_gt_u32_e64 s[46:47], v173, v170
	v_addc_co_u32_e32 v168, vcc, 0, v168, vcc
	v_addc_co_u32_e64 v169, s[40:41], 0, v169, s[40:41]
	v_addc_co_u32_e64 v168, s[46:47], 0, v168, s[46:47]
	v_cmp_gt_u32_e32 vcc, v177, v163
	v_cmp_gt_u32_e64 s[40:41], v174, v170
	v_cmp_gt_u32_e64 s[46:47], v178, v163
	v_addc_co_u32_e32 v169, vcc, 0, v169, vcc
	v_addc_co_u32_e64 v168, s[40:41], 0, v168, s[40:41]
	v_addc_co_u32_e64 v169, s[46:47], 0, v169, s[46:47]
	s_waitcnt lgkmcnt(4)
	v_cmp_gt_u32_e32 vcc, v175, v170
	v_cmp_gt_u32_e64 s[40:41], v179, v163
	v_cmp_gt_u32_e64 s[46:47], v182, v170
	v_addc_co_u32_e32 v168, vcc, 0, v168, vcc
	v_addc_co_u32_e64 v169, s[40:41], 0, v169, s[40:41]
	v_addc_co_u32_e64 v168, s[46:47], 0, v168, s[46:47]
	v_cmp_gt_u32_e32 vcc, v186, v163
	v_cmp_gt_u32_e64 s[40:41], v183, v170
	v_cmp_gt_u32_e64 s[46:47], v187, v163
	v_addc_co_u32_e32 v169, vcc, 0, v169, vcc
	v_addc_co_u32_e64 v168, s[40:41], 0, v168, s[40:41]
	v_addc_co_u32_e64 v169, s[46:47], 0, v169, s[46:47]
	v_cmp_gt_u32_e32 vcc, v184, v170
	v_cmp_gt_u32_e64 s[40:41], v188, v163
	v_cmp_gt_u32_e64 s[46:47], v185, v170
	v_addc_co_u32_e32 v168, vcc, 0, v168, vcc
	v_addc_co_u32_e64 v169, s[40:41], 0, v169, s[40:41]
	v_addc_co_u32_e64 v168, s[46:47], 0, v168, s[46:47]
	s_waitcnt lgkmcnt(2)
	v_cmp_gt_u32_e32 vcc, v189, v163
	v_cmp_gt_u32_e64 s[40:41], v190, v170
	v_cmp_gt_u32_e64 s[46:47], v194, v163
	v_addc_co_u32_e32 v169, vcc, 0, v169, vcc
	v_addc_co_u32_e64 v168, s[40:41], 0, v168, s[40:41]
	v_addc_co_u32_e64 v169, s[46:47], 0, v169, s[46:47]
	v_cmp_gt_u32_e32 vcc, v191, v170
	v_cmp_gt_u32_e64 s[40:41], v195, v163
	v_cmp_gt_u32_e64 s[46:47], v192, v170
	v_addc_co_u32_e32 v168, vcc, 0, v168, vcc
	v_addc_co_u32_e64 v169, s[40:41], 0, v169, s[40:41]
	v_addc_co_u32_e64 v168, s[46:47], 0, v168, s[46:47]
	v_cmp_gt_u32_e32 vcc, v196, v163
	v_cmp_gt_u32_e64 s[40:41], v193, v170
	v_cmp_gt_u32_e64 s[46:47], v197, v163
	v_addc_co_u32_e32 v169, vcc, 0, v169, vcc
	v_addc_co_u32_e64 v168, s[40:41], 0, v168, s[40:41]
	v_addc_co_u32_e64 v169, s[46:47], 0, v169, s[46:47]
	s_waitcnt lgkmcnt(0)
	v_cmp_gt_u32_e32 vcc, v202, v170
	v_cmp_gt_u32_e64 s[40:41], v206, v163
	v_cmp_gt_u32_e64 s[46:47], v203, v170
	v_addc_co_u32_e32 v168, vcc, 0, v168, vcc
	v_addc_co_u32_e64 v169, s[40:41], 0, v169, s[40:41]
	v_addc_co_u32_e64 v168, s[46:47], 0, v168, s[46:47]
	v_cmp_gt_u32_e32 vcc, v207, v163
	v_cmp_gt_u32_e64 s[40:41], v204, v170
	v_cmp_gt_u32_e64 s[46:47], v208, v163
	v_addc_co_u32_e32 v169, vcc, 0, v169, vcc
	v_addc_co_u32_e64 v168, s[40:41], 0, v168, s[40:41]
	v_addc_co_u32_e64 v169, s[46:47], 0, v169, s[46:47]
	v_cmp_gt_u32_e32 vcc, v205, v170
	v_cmp_gt_u32_e64 s[40:41], v209, v163
	s_nop 0
	v_addc_co_u32_e32 v168, vcc, 0, v168, vcc
	v_addc_co_u32_e64 v169, s[40:41], 0, v169, s[40:41]
	v_cmp_gt_u32_e64 s[40:41], 8, v168
	v_mov_b32_e32 v166, v181
	s_nop 0
	v_cndmask_b32_e64 v162, 0, v165, s[40:41]
	s_nop 1
	v_add_f32_dpp v162, v162, v162 row_shr:1 row_mask:0xf bank_mask:0xf bound_ctrl:1
	s_nop 1
	v_add_f32_dpp v162, v162, v162 row_shr:2 row_mask:0xf bank_mask:0xf bound_ctrl:1
	s_nop 1
	v_add_f32_dpp v162, v162, v162 row_shr:4 row_mask:0xf bank_mask:0xf bound_ctrl:1
	s_nop 1
	v_add_f32_dpp v162, v162, v162 row_shr:8 row_mask:0xf bank_mask:0xf bound_ctrl:1
	s_nop 1
	v_mov_b32_dpp v166, v162 row_bcast:15 row_mask:0xa bank_mask:0xf
	v_add_f32_e32 v162, v162, v166
	v_mov_b32_e32 v166, v181
	s_nop 1
	v_mov_b32_dpp v166, v162 row_bcast:31 row_mask:0xc bank_mask:0xf
	v_add_f32_e32 v162, v162, v166
	s_nop 0
	v_readlane_b32 s2, v162, 63
	v_mov_b32_e32 v162, -1
	s_and_saveexec_b64 s[0:1], s[40:41]
	ds_add_u32 v223, v216
	v_mov_b32_e32 v180, v168
	s_or_b64 exec, exec, s[0:1]
	v_cmp_gt_u32_e32 vcc, 8, v169
	v_mov_b32_e32 v166, v181
	s_nop 0
	v_cndmask_b32_e32 v167, 0, v164, vcc
	s_nop 1
	v_add_f32_dpp v167, v167, v167 row_shr:1 row_mask:0xf bank_mask:0xf bound_ctrl:1
	s_nop 1
	v_add_f32_dpp v167, v167, v167 row_shr:2 row_mask:0xf bank_mask:0xf bound_ctrl:1
	s_nop 1
	v_add_f32_dpp v167, v167, v167 row_shr:4 row_mask:0xf bank_mask:0xf bound_ctrl:1
	s_nop 1
	v_add_f32_dpp v167, v167, v167 row_shr:8 row_mask:0xf bank_mask:0xf bound_ctrl:1
	s_nop 1
	v_mov_b32_dpp v166, v167 row_bcast:15 row_mask:0xa bank_mask:0xf
	v_add_f32_e32 v167, v167, v166
	v_mov_b32_e32 v166, v181
	s_nop 1
	v_mov_b32_dpp v166, v167 row_bcast:31 row_mask:0xc bank_mask:0xf
	v_add_f32_e32 v167, v167, v166
	s_nop 0
	v_readlane_b32 s3, v167, 63
	s_and_saveexec_b64 s[0:1], vcc
	s_cbranch_execz .LBB0_1285
	ds_add_u32 v223, v216
	v_mov_b32_e32 v162, v169
	s_branch .LBB0_1285
